# zero-state offload + chain prologue waits only for its decay load (vmcnt 8) + tile-1 staging before first wait in all 11 gemm prologues + barrier leader reorder
# baseline (speedup 1.0000x reference)
.LBB0_697:
	s_lshl_b32 s10, s10, 5
	s_sub_i32 s13, 6, s74
	s_add_i32 s26, s74, 1
	v_lshrrev_b32_e32 v19, 1, v17
	s_and_b64 s[14:15], s[36:37], exec
	v_and_b32_e32 v32, 24, v19
	s_cselect_b32 s13, s26, s13
	v_and_b32_e32 v18, 15, v17
	v_lshlrev_b32_e32 v19, 1, v32
	v_lshlrev_b32_e32 v34, 2, v17
	s_add_i32 s13, s13, s12
	s_waitcnt vmcnt(8)
	v_mul_f32_e32 v17, 0xbfb8aa3b, v16
	v_lshl_or_b32 v210, s9, 6, v18
	v_lshl_or_b32 v33, v18, 6, v19
	s_lshl_b32 s12, s13, 9
	v_rndne_f32_e32 v18, v17
	s_mov_b32 s13, 0xbfb8aa3b
	v_sub_f32_e32 v19, v17, v18
	v_fma_f32 v17, v16, s13, -v17
	v_fmac_f32_e32 v17, 0xb2a5705f, v16
	v_add_f32_e32 v17, v19, v17
	v_exp_f32_e32 v17, v17
	v_cvt_i32_f32_e32 v18, v18
	s_or_b32 s48, s12, s11
	s_mov_b32 s11, 0x42ce8ed0
	s_and_b32 s10, s10, 0x60
	v_ldexp_f32 v17, v17, v18
	v_cmp_nlt_f32_e32 vcc, s11, v16
	s_mov_b32 s11, 0xc2b17218
	s_add_i32 m0, s7, 0x18000
	v_lshl_add_u64 v[8:9], v[8:9], 0, s[82:83]
	s_lshl_b32 s9, s9, 13
	s_lshl_b32 s14, s10, 7
	v_cndmask_b32_e32 v17, 0, v17, vcc
	v_cmp_ngt_f32_e32 vcc, s11, v16
	global_load_lds_dwordx4 v[8:9], off
	v_lshl_add_u64 v[6:7], v[6:7], 0, s[82:83]
	s_add_i32 m0, s7, 0x1a000
	s_add_i32 s87, s7, 0x8000
	s_add_i32 s88, s7, 0xa000
	v_cndmask_b32_e32 v35, v252, v17, vcc
	global_load_lds_dwordx4 v[6:7], off
	v_lshl_add_u64 v[2:3], v[2:3], 0, s[60:61]
	s_mov_b32 m0, s87
	s_add_u32 s12, s54, 0x20800
	v_add_f32_e32 v18, 1.0, v35
	global_load_lds_dwordx4 v[2:3], off
	v_lshl_add_u64 v[2:3], v[4:5], 0, s[60:61]
	s_mov_b32 m0, s88
	s_addc_u32 s13, s55, 0
	v_add_f32_e32 v16, -1.0, v18
	global_load_lds_dwordx4 v[2:3], off
	s_add_i32 m0, s7, 0x1c000
	v_lshl_add_u64 v[2:3], s[12:13], 0, v[200:201]
	v_sub_f32_e32 v17, v16, v18
	global_load_lds_dwordx4 v[2:3], off
	v_lshl_add_u64 v[2:3], s[12:13], 0, v[208:209]
	s_add_i32 m0, s7, 0x1e000
	v_add_f32_e32 v17, 1.0, v17
	v_sub_f32_e32 v16, v35, v16
	global_load_lds_dwordx4 v[2:3], off
	s_mov_b64 vcc, s[40:41]
	s_cbranch_vccz .Lpro_skip_4
	s_barrier
.Lpro_skip_4:
	s_waitcnt vmcnt(8)
	s_barrier
	v_add_f32_e32 v19, v16, v17
	v_frexp_mant_f32_e32 v20, v18
	v_cvt_f64_f32_e32 v[16:17], v18
	s_mov_b32 s11, 0x3f2aaaab
	v_frexp_exp_i32_f64_e32 v16, v[16:17]
	v_cmp_gt_f32_e32 vcc, s11, v20
	s_mov_b32 s11, 0x3f317218
	v_lshlrev_b32_e32 v3, 14, v10
	v_subbrev_co_u32_e32 v24, vcc, 0, v16, vcc
	v_sub_u32_e32 v16, 0, v24
	v_ldexp_f32 v17, v18, v16
	v_add_f32_e32 v18, -1.0, v17
	v_add_f32_e32 v20, 1.0, v17
	v_ldexp_f32 v16, v19, v16
	v_add_f32_e32 v19, 1.0, v18
	v_add_f32_e32 v21, -1.0, v20
	v_sub_f32_e32 v19, v17, v19
	v_sub_f32_e32 v17, v17, v21
	v_add_f32_e32 v19, v16, v19
	v_add_f32_e32 v16, v16, v17
	v_add_f32_e32 v25, v20, v16
	v_rcp_f32_e32 v27, v25
	v_sub_f32_e32 v17, v20, v25
	v_add_f32_e32 v26, v16, v17
	v_add_f32_e32 v17, v18, v19
	v_mul_f32_e32 v29, v17, v27
	v_sub_f32_e32 v16, v18, v17
	v_mul_f32_e32 v18, v25, v29
	v_fma_f32 v20, v29, v25, -v18
	v_fmac_f32_e32 v20, v29, v26
	v_add_f32_e32 v28, v19, v16
	v_add_f32_e32 v16, v18, v20
	v_sub_f32_e32 v19, v17, v16
	v_pk_add_f32 v[22:23], v[16:17], v[18:19] neg_lo:[0,1] neg_hi:[0,1]
	v_mov_b32_e32 v21, v16
	v_pk_add_f32 v[16:17], v[22:23], v[20:21] neg_lo:[0,1] neg_hi:[0,1]
	v_and_b32_e32 v3, 0xffff8000, v3
	v_add_f32_e32 v17, v28, v17
	v_add_f32_e32 v16, v16, v17
	v_add_f32_e32 v17, v19, v16
	v_mul_f32_e32 v28, v27, v17
	v_mul_f32_e32 v18, v25, v28
	v_fma_f32 v20, v28, v25, -v18
	v_fmac_f32_e32 v20, v28, v26
	v_sub_f32_e32 v19, v19, v17
	v_add_f32_e32 v25, v16, v19
	v_add_f32_e32 v16, v18, v20
	v_sub_f32_e32 v19, v17, v16
	v_pk_add_f32 v[22:23], v[16:17], v[18:19] neg_lo:[0,1] neg_hi:[0,1]
	v_mov_b32_e32 v21, v16
	v_pk_add_f32 v[16:17], v[22:23], v[20:21] neg_lo:[0,1] neg_hi:[0,1]
	v_lshl_add_u32 v3, v11, 11, v3
	v_add_f32_e32 v17, v25, v17
	v_add_f32_e32 v16, v16, v17
	v_add_f32_e32 v17, v29, v28
	v_add_f32_e32 v16, v19, v16
	v_sub_f32_e32 v18, v17, v29
	v_mul_f32_e32 v16, v27, v16
	v_sub_f32_e32 v18, v28, v18
	v_add_f32_e32 v18, v18, v16
	v_add_f32_e32 v20, v17, v18
	v_mul_f32_e32 v21, v20, v20
	v_fmamk_f32 v16, v21, 0x3e9b6dac, v248
	v_fmaak_f32 v205, v21, v16, 0x3f2aaada
	v_cvt_f32_i32_e32 v16, v24
	v_sub_f32_e32 v17, v20, v17
	v_sub_f32_e32 v17, v18, v17
	v_ldexp_f32 v22, v17, 1
	v_mul_f32_e32 v17, v20, v21
	v_ldexp_f32 v19, v20, 1
	v_pk_mul_f32 v[20:21], v[16:17], v[204:205]
	v_and_b32_e32 v4, 1, v10
	v_fma_f32 v18, v16, s11, -v20
	v_fmac_f32_e32 v18, 0xb102e308, v16
	v_pk_add_f32 v[16:17], v[20:21], v[18:19]
	s_mov_b32 s11, 0x7f800000
	v_sub_f32_e32 v19, v17, v19
	v_sub_f32_e32 v19, v21, v19
	v_add_f32_e32 v23, v22, v19
	v_mov_b32_e32 v22, v20
	v_pk_add_f32 v[20:21], v[16:17], v[20:21] neg_lo:[0,1] neg_hi:[0,1]
	v_pk_add_f32 v[24:25], v[16:17], v[22:23]
	v_mov_b32_e32 v19, v16
	v_mov_b32_e32 v21, v25
	v_pk_add_f32 v[26:27], v[18:19], v[20:21] neg_lo:[0,1] neg_hi:[0,1]
	v_pk_add_f32 v[18:19], v[18:19], v[20:21]
	v_mov_b32_e32 v30, v17
	v_pk_add_f32 v[20:21], v[18:19], v[16:17] op_sel:[1,0] op_sel_hi:[0,1] neg_lo:[0,1] neg_hi:[0,1]
	v_pk_add_f32 v[28:29], v[24:25], v[20:21] op_sel_hi:[1,0] neg_lo:[0,1] neg_hi:[0,1]
	v_mov_b32_e32 v24, v25
	v_mov_b32_e32 v25, v19
	v_mov_b32_e32 v31, v20
	v_pk_add_f32 v[20:21], v[24:25], v[30:31] neg_lo:[0,1] neg_hi:[0,1]
	v_mov_b32_e32 v22, v23
	v_mov_b32_e32 v23, v16
	v_pk_add_f32 v[16:17], v[22:23], v[20:21] neg_lo:[0,1] neg_hi:[0,1]
	v_mov_b32_e32 v28, v26
	v_pk_add_f32 v[20:21], v[28:29], v[16:17]
	v_mov_b32_e32 v27, v19
	v_pk_add_f32 v[22:23], v[20:21], v[20:21] op_sel:[0,1] op_sel_hi:[1,0]
	v_cmp_neq_f32_e32 vcc, s11, v35
	v_pk_add_f32 v[18:19], v[18:19], v[22:23] op_sel:[1,0] op_sel_hi:[0,1]
	v_mov_b32_e32 v21, v18
	v_pk_add_f32 v[24:25], v[20:21], v[26:27] neg_lo:[0,1] neg_hi:[0,1]
	v_mov_b32_e32 v17, v22
	v_sub_f32_e32 v19, v20, v24
	v_pk_add_f32 v[16:17], v[16:17], v[24:25] neg_lo:[0,1] neg_hi:[0,1]
	v_sub_f32_e32 v19, v26, v19
	v_add_f32_e32 v16, v16, v19
	v_add_f32_e32 v16, v16, v17
	v_add_f32_e32 v16, v18, v16
	s_mov_b32 s11, 0x33800000
	v_cndmask_b32_e32 v16, v252, v16, vcc
	v_cmp_lt_f32_e64 vcc, |v35|, s11
	v_lshl_or_b32 v3, v4, 6, v3
	v_lshl_add_u32 v232, v12, 1, v3
	v_cndmask_b32_e32 v16, v16, v35, vcc
	v_mul_f32_e32 v2, 0xbfb8aa3b, v16
	v_mul_f32_e32 v2, 0x44000000, v2
	v_lshlrev_b32_e32 v3, 14, v13
	v_exp_f32_e32 v212, v2
	v_and_b32_e32 v3, 0xffff8000, v3
	v_and_b32_e32 v2, 32, v34
	v_lshl_add_u32 v3, v14, 11, v3
	v_and_b32_e32 v4, 1, v13
	v_bitop3_b32 v205, v33, s14, v2 bitop3:0xde
	v_bitop3_b32 v2, v33, s9, v2 bitop3:0xde
	s_waitcnt vmcnt(6)
	v_lshl_or_b32 v3, v4, 6, v3
	v_mov_b32_e32 v66, v67
	v_mov_b32_e32 v68, v67
	v_mov_b32_e32 v69, v67
	s_cmpk_lt_u32 s8, 0x100
	v_or_b32_e32 v216, s10, v32
	v_or_b32_e32 v218, 16, v210
	v_or_b32_e32 v220, 32, v210
	v_or_b32_e32 v222, 48, v210
	v_add_u32_e32 v224, 0x80, v210
	v_add_u32_e32 v226, 0x90, v210
	v_add_u32_e32 v228, 0xa0, v210
	v_add_u32_e32 v230, 0xb0, v210
	v_lshl_add_u32 v234, v15, 1, v3
	v_add_u32_e32 v217, 0, v2
	v_mov_b64_e32 v[2:3], v[66:67]
	v_mov_b64_e32 v[6:7], v[66:67]
	v_mov_b64_e32 v[10:11], v[66:67]
	v_mov_b64_e32 v[14:15], v[66:67]
	v_mov_b64_e32 v[18:19], v[66:67]
	v_mov_b64_e32 v[22:23], v[66:67]
	v_mov_b64_e32 v[26:27], v[66:67]
	v_mov_b64_e32 v[30:31], v[66:67]
	v_mov_b64_e32 v[34:35], v[66:67]
	v_mov_b64_e32 v[38:39], v[66:67]
	v_mov_b64_e32 v[42:43], v[66:67]
	v_mov_b64_e32 v[46:47], v[66:67]
	v_mov_b64_e32 v[50:51], v[66:67]
	v_mov_b64_e32 v[54:55], v[66:67]
	v_mov_b64_e32 v[58:59], v[66:67]
	v_mov_b64_e32 v[62:63], v[66:67]
	v_mov_b64_e32 v[72:73], v[68:69]
	v_mov_b64_e32 v[76:77], v[68:69]
	v_mov_b64_e32 v[80:81], v[68:69]
	v_mov_b64_e32 v[84:85], v[68:69]
	v_mov_b64_e32 v[88:89], v[68:69]
	v_mov_b64_e32 v[92:93], v[68:69]
	v_mov_b64_e32 v[96:97], v[68:69]
	v_mov_b64_e32 v[100:101], v[68:69]
	v_mov_b64_e32 v[104:105], v[68:69]
	v_mov_b64_e32 v[108:109], v[68:69]
	v_mov_b64_e32 v[112:113], v[68:69]
	v_mov_b64_e32 v[116:117], v[68:69]
	v_mov_b64_e32 v[120:121], v[68:69]
	v_mov_b64_e32 v[124:125], v[68:69]
	v_mov_b64_e32 v[128:129], v[68:69]
	v_mov_b64_e32 v[132:133], v[68:69]
	v_mov_b32_e32 v214, v212
	v_mov_b32_e32 v215, v212
	s_cselect_b64 s[42:43], -1, 0
	v_ashrrev_i32_e32 v211, 31, v210
	v_ashrrev_i32_e32 v219, 31, v218
	v_ashrrev_i32_e32 v221, 31, v220
	v_ashrrev_i32_e32 v223, 31, v222
	v_ashrrev_i32_e32 v225, 31, v224
	v_ashrrev_i32_e32 v227, 31, v226
	v_ashrrev_i32_e32 v229, 31, v228
	v_ashrrev_i32_e32 v231, 31, v230
	v_mov_b32_e32 v233, v67
	v_mov_b32_e32 v235, v67
	s_mov_b64 s[36:37], 0
	v_mov_b64_e32 v[4:5], v[68:69]
	v_mov_b64_e32 v[8:9], v[68:69]
	v_mov_b64_e32 v[12:13], v[68:69]
	v_mov_b64_e32 v[16:17], v[68:69]
	v_mov_b64_e32 v[20:21], v[68:69]
	v_mov_b64_e32 v[24:25], v[68:69]
	v_mov_b64_e32 v[28:29], v[68:69]
	v_mov_b64_e32 v[32:33], v[68:69]
	v_mov_b64_e32 v[36:37], v[68:69]
	v_mov_b64_e32 v[40:41], v[68:69]
	v_mov_b64_e32 v[44:45], v[68:69]
	v_mov_b64_e32 v[48:49], v[68:69]
	v_mov_b64_e32 v[52:53], v[68:69]
	v_mov_b64_e32 v[56:57], v[68:69]
	v_mov_b64_e32 v[60:61], v[68:69]
	v_mov_b64_e32 v[64:65], v[68:69]
	v_mov_b64_e32 v[70:71], v[66:67]
	v_mov_b64_e32 v[74:75], v[66:67]
	v_mov_b64_e32 v[78:79], v[66:67]
	v_mov_b64_e32 v[82:83], v[66:67]
	v_mov_b64_e32 v[86:87], v[66:67]
	v_mov_b64_e32 v[90:91], v[66:67]
	v_mov_b64_e32 v[94:95], v[66:67]
	v_mov_b64_e32 v[98:99], v[66:67]
	v_mov_b64_e32 v[102:103], v[66:67]
	v_mov_b64_e32 v[106:107], v[66:67]
	v_mov_b64_e32 v[110:111], v[66:67]
	v_mov_b64_e32 v[114:115], v[66:67]
	v_mov_b64_e32 v[118:119], v[66:67]
	v_mov_b64_e32 v[122:123], v[66:67]
	v_mov_b64_e32 v[126:127], v[66:67]
	v_mov_b64_e32 v[130:131], v[66:67]
	s_barrier
	s_branch .LBB0_700
